# code placement: hot loop heads (GEMM main loops, MLA and stick-breaking key loops) aligned to 64 bytes
# speedup vs baseline: 1.0036x; 1.0032x over previous
;     __device__ bool next(int i, Unit& u) const { const int L = i * G + c; if (L >= 256) return false; u.pm = L >> 2; u.pn = L & 3; u.pb = 16; u.e = 0; u.ko = (L & 3) * 1024; u.ui = i; return true; }
;     ...
;     for (;;) {
;         const bool has_next = S.next(ui + 1, nxt);
;         const char* nB = has_next ? (const char*)Bt + (size_t)nxt.pb * tstep + nxt.ko : (chain ? cBn : cB);
;         int t0 = 0;
;         if (Epi::NST > 0 && ui > 0) { PG_KPAIR(0, 8 + Epi::NST); t0 = 2; }
;         for (int t = t0; t < nt; t += 2) PG_KPAIR(t, 8);
.LBB0_318:
	v_mov_b32_e32 v218, v198
	v_mov_b32_e32 v220, v231
	v_mov_b32_e32 v219, v233
	v_mov_b32_e32 v221, v232
	.p2alignl 6, 3212836864

;     __device__ bool next(int i, Unit& u) const { const int L = i * G + c; if (L >= 256) return false; u.pm = L >> 2; u.pn = L & 3; u.pb = 16; u.e = 0; u.ko = (L & 3) * 1024; u.ui = i; return true; }
;     ...
;     for (;;) {
;         const bool has_next = S.next(ui + 1, nxt);
;         const char* nB = has_next ? (const char*)Bt + (size_t)nxt.pb * tstep + nxt.ko : (chain ? cBn : cB);
;         int t0 = 0;
;         if (Epi::NST > 0 && ui > 0) { PG_KPAIR(0, 8 + Epi::NST); t0 = 2; }
;         for (int t = t0; t < nt; t += 2) PG_KPAIR(t, 8);
.LBB0_368:
	v_mov_b32_e32 v215, v198
	v_mov_b32_e32 v217, v226
	v_mov_b32_e32 v216, v225
	v_mov_b32_e32 v218, v227
	.p2alignl 6, 3212836864

;     __device__ bool next(int i, Unit& u) const { const int L = i * G + c; if (L >= 256) return false; u.pm = L >> 2; u.pn = L & 3; u.pb = 16; u.e = 0; u.ko = (L & 3) * 1024; u.ui = i; return true; }
;     ...
;         const bool has_next = S.next(ui + 1, nxt);
;         const char* nB = has_next ? (const char*)Bt + (size_t)nxt.pb * tstep + nxt.ko : (chain ? cBn : cB);
;         int t0 = 0;
;         if (Epi::NST > 0 && ui > 0) { PG_KPAIR(0, 8 + Epi::NST); t0 = 2; }
;         for (int t = t0; t < nt; t += 2) PG_KPAIR(t, 8);
;         E(acc, cur, wr, wc, fr, fq);
;         if (!has_next) break;
; #pragma unroll
;         for (int a = 0; a < 2; ++a)
; #pragma unroll
;             for (int b = 0; b < 2; ++b)
; #pragma unroll
;                 for (int m = 0; m < 4; ++m)
; #pragma unroll
;                     for (int n = 0; n < 2; ++n) acc[a][b][m][n] = (f32x4){0.f, 0.f, 0.f, 0.f};
;         cur = nxt; cB = nB; ++ui;
.LBB0_387:
	s_add_i32 s51, s51, 1
	s_mov_b64 s[22:23], s[4:5]
	s_mul_i32 s4, s51, s76
	s_add_i32 s4, s4, s70
	s_cmpk_gt_i32 s4, 0xff
	s_mov_b32 s6, s30
	s_cselect_b64 s[20:21], -1, 0
	s_and_b32 s30, s4, 3
	s_mov_b32 s24, s31
	s_mov_b32 s53, s31
	s_mov_b32 s25, s52
	s_lshl_b32 s52, s30, 10
	s_ashr_i32 s31, s4, 2
	s_and_b64 s[4:5], s[20:21], exec
	s_cselect_b32 s26, s25, s52
	s_cselect_b32 s27, s24, s31
	s_ashr_i32 s5, s26, 31
	s_add_u32 s4, s33, s26
	s_addc_u32 s5, s34, s5
	v_lshl_or_b32 v2, s27, 8, v202
	s_and_b64 s[24:25], s[20:21], exec
	v_add_u32_e32 v3, s26, v1
	v_or_b32_e32 v4, v2, v118
	v_or_b32_e32 v2, v2, v119
	s_cselect_b32 s54, s23, s5
	s_cselect_b32 s55, s22, s4
	v_lshl_add_u32 v127, v4, 12, v3
	v_lshl_add_u32 v129, v2, 12, v3
	s_add_u32 s56, s22, 0x100
	v_add_u32_e32 v128, 0x80000, v127
	v_add_u32_e32 v130, 0x80000, v129
	s_addc_u32 s57, s23, 0
	s_mov_b32 s58, -2
	s_mov_b64 s[22:23], 0
	v_mov_b32_e32 v2, 0
	v_mov_b32_e32 v3, v115
	v_mov_b32_e32 v4, v115
	v_mov_b32_e32 v5, v115
	v_mov_b32_e32 v6, 0
	v_mov_b32_e32 v7, v115
	v_mov_b32_e32 v8, v115
	v_mov_b32_e32 v9, v115
	v_mov_b32_e32 v10, 0
	v_mov_b32_e32 v11, v115
	v_mov_b32_e32 v12, v115
	v_mov_b32_e32 v13, v115
	v_mov_b32_e32 v14, 0
	v_mov_b32_e32 v15, v115
	v_mov_b32_e32 v16, v115
	v_mov_b32_e32 v17, v115
	v_mov_b32_e32 v18, 0
	v_mov_b32_e32 v19, v115
	v_mov_b32_e32 v20, v115
	v_mov_b32_e32 v21, v115
	v_mov_b32_e32 v22, 0
	v_mov_b32_e32 v23, v115
	v_mov_b32_e32 v24, v115
	v_mov_b32_e32 v25, v115
	v_mov_b32_e32 v26, 0
	v_mov_b32_e32 v27, v115
	v_mov_b32_e32 v28, v115
	v_mov_b32_e32 v29, v115
	v_mov_b32_e32 v30, 0
	v_mov_b32_e32 v31, v115
	v_mov_b32_e32 v32, v115
	v_mov_b32_e32 v33, v115
	v_mov_b32_e32 v34, 0
	v_mov_b32_e32 v35, v115
	v_mov_b32_e32 v36, v115
	v_mov_b32_e32 v37, v115
	v_mov_b32_e32 v38, 0
	v_mov_b32_e32 v39, v115
	v_mov_b32_e32 v40, v115
	v_mov_b32_e32 v41, v115
	v_mov_b32_e32 v42, 0
	v_mov_b32_e32 v43, v115
	v_mov_b32_e32 v44, v115
	v_mov_b32_e32 v45, v115
	v_mov_b32_e32 v46, 0
	v_mov_b32_e32 v47, v115
	v_mov_b32_e32 v48, v115
	v_mov_b32_e32 v49, v115
	v_mov_b32_e32 v50, 0
	v_mov_b32_e32 v51, v115
	v_mov_b32_e32 v52, v115
	v_mov_b32_e32 v53, v115
	v_mov_b32_e32 v54, 0
	v_mov_b32_e32 v55, v115
	v_mov_b32_e32 v56, v115
	v_mov_b32_e32 v57, v115
	v_mov_b32_e32 v58, 0
	v_mov_b32_e32 v59, v115
	v_mov_b32_e32 v60, v115
	v_mov_b32_e32 v61, v115
	v_mov_b32_e32 v62, 0
	v_mov_b32_e32 v63, v115
	v_mov_b32_e32 v64, v115
	v_mov_b32_e32 v65, v115
	.p2alignl 6, 3212836864

;     __device__ bool next(int i, Unit& u) const { const int L = i * G + c; if (L >= 256) return false; u.pm = L >> 2; u.pn = L & 3; u.pb = 16; u.e = 0; u.ko = (L & 3) * 1024; u.ui = i; return true; }
;     ...
;     for (;;) {
;         const bool has_next = S.next(ui + 1, nxt);
;         const char* nB = has_next ? (const char*)Bt + (size_t)nxt.pb * tstep + nxt.ko : (chain ? cBn : cB);
;         int t0 = 0;
;         if (Epi::NST > 0 && ui > 0) { PG_KPAIR(0, 8 + Epi::NST); t0 = 2; }
;         for (int t = t0; t < nt; t += 2) PG_KPAIR(t, 8);
.LBB0_484:
	v_mov_b32_e32 v221, v198
	v_mov_b32_e32 v223, v235
	v_mov_b32_e32 v222, v234
	v_mov_b32_e32 v224, v236
	.p2alignl 6, 3212836864

;     __device__ bool next(int i, Unit& u) const { const int L = i * G + c; if (L >= 256) return false; u.pm = L >> 2; u.pn = L & 3; u.pb = 16; u.e = 0; u.ko = (L & 3) * 1024; u.ui = i; return true; }
;     ...
;     for (;;) {
;         const bool has_next = S.next(ui + 1, nxt);
;         const char* nB = has_next ? (const char*)Bt + (size_t)nxt.pb * tstep + nxt.ko : (chain ? cBn : cB);
;         int t0 = 0;
;         if (Epi::NST > 0 && ui > 0) { PG_KPAIR(0, 8 + Epi::NST); t0 = 2; }
;         for (int t = t0; t < nt; t += 2) PG_KPAIR(t, 8);
.LBB0_546:
	v_mov_b32_e32 v215, v228
	v_mov_b32_e32 v217, v230
	v_mov_b32_e32 v216, v229
	v_mov_b32_e32 v218, v231
	.p2alignl 6, 3212836864

;     __device__ bool next(int i, Unit& u) const { const int L = i * G + c; if (L >= 256) return false; u.pm = L >> 2; u.pn = L & 3; u.pb = 16; u.e = 0; u.ko = (L & 3) * 1024; u.ui = i; return true; }
;     __device__ bool next(int i, Unit& u) const {
;         const long L = (long)i * G + c; if (L >= nwg) return false;
;         int wgid = (int)L; { const int q = nwg / NXCD, r = nwg % NXCD, xcd = wgid % NXCD, off = wgid / NXCD; wgid = (xcd < r ? xcd * (q + 1) : r * (q + 1) + (xcd - r) * q) + off; }
;         const int nig = WGM * nN, gid = wgid / nig, fm = gid * WGM, gsz = (nM - fm) < WGM ? (nM - fm) : WGM;
;         u.pm = fm + ((wgid % nig) % gsz); u.pn = (wgid % nig) / gsz; u.pb = u.pn >= skip_from ? u.pn + skip_by : u.pn; u.e = 0; u.ko = 0; u.ui = i; return true;
;     ...
;     for (;;) {
;         const bool has_next = S.next(ui + 1, nxt);
;         const char* nB = has_next ? (const char*)Bt + (size_t)nxt.pb * tstep + nxt.ko : (chain ? cBn : cB);
;         int t0 = 0;
;         if (Epi::NST > 0 && ui > 0) { PG_KPAIR(0, 8 + Epi::NST); t0 = 2; }
;         for (int t = t0; t < nt; t += 2) PG_KPAIR(t, 8);
;         E(acc, cur, wr, wc, fr, fq);
;         if (!has_next) break;
; #pragma unroll
;         for (int a = 0; a < 2; ++a)
; #pragma unroll
;             for (int b = 0; b < 2; ++b)
; #pragma unroll
;                 for (int m = 0; m < 4; ++m)
; #pragma unroll
;                     for (int n = 0; n < 2; ++n) acc[a][b][m][n] = (f32x4){0.f, 0.f, 0.f, 0.f};
;         cur = nxt; cB = nB; ++ui;
.LBB0_575:
	s_ashr_i32 s21, s20, 31
	s_lshl_b64 s[6:7], s[20:21], 18
	s_add_u32 s22, s16, s6
	v_lshl_or_b32 v2, s53, 8, v206
	s_addc_u32 s23, s17, s7
	v_or_b32_e32 v3, v2, v198
	v_or_b32_e32 v2, v2, v199
	s_and_b64 s[6:7], exec, s[4:5]
	v_lshlrev_b32_e32 v2, 10, v2
	s_cselect_b32 s21, s1, s23
	s_cselect_b32 s40, s0, s22
	v_lshl_or_b32 v196, v3, 10, v202
	v_or_b32_e32 v220, v2, v202
	v_add_u32_e32 v221, v2, v209
	s_add_u32 s41, s0, 0x100
	v_mov_b32_e32 v2, 0
	v_or_b32_e32 v219, 0x20000, v196
	s_addc_u32 s54, s1, 0
	s_mov_b32 s55, -2
	s_mov_b64 s[0:1], 0
	v_mov_b32_e32 v3, v2
	v_mov_b32_e32 v4, v2
	v_mov_b32_e32 v5, v2
	s_waitcnt vmcnt(4)
	v_mov_b32_e32 v6, v2
	v_mov_b32_e32 v7, v2
	v_mov_b32_e32 v8, v2
	v_mov_b32_e32 v9, v2
	s_waitcnt vmcnt(3)
	v_mov_b32_e32 v10, v2
	v_mov_b32_e32 v11, v2
	v_mov_b32_e32 v12, v2
	v_mov_b32_e32 v13, v2
	s_waitcnt vmcnt(2)
	v_mov_b32_e32 v14, v2
	v_mov_b32_e32 v15, v2
	v_mov_b32_e32 v16, v2
	v_mov_b32_e32 v17, v2
	v_mov_b32_e32 v18, v2
	v_mov_b32_e32 v19, v2
	v_mov_b32_e32 v20, v2
	v_mov_b32_e32 v21, v2
	v_mov_b32_e32 v22, v2
	v_mov_b32_e32 v23, v2
	v_mov_b32_e32 v24, v2
	v_mov_b32_e32 v25, v2
	v_mov_b32_e32 v26, v2
	v_mov_b32_e32 v27, v2
	v_mov_b32_e32 v28, v2
	v_mov_b32_e32 v29, v2
	v_mov_b32_e32 v30, v2
	v_mov_b32_e32 v31, v2
	v_mov_b32_e32 v32, v2
	v_mov_b32_e32 v33, v2
	v_mov_b32_e32 v66, v2
	v_mov_b32_e32 v67, v2
	v_mov_b32_e32 v68, v2
	v_mov_b32_e32 v69, v2
	v_mov_b32_e32 v70, v2
	v_mov_b32_e32 v71, v2
	v_mov_b32_e32 v72, v2
	v_mov_b32_e32 v73, v2
	v_mov_b32_e32 v74, v2
	v_mov_b32_e32 v75, v2
	v_mov_b32_e32 v76, v2
	v_mov_b32_e32 v77, v2
	v_mov_b32_e32 v78, v2
	v_mov_b32_e32 v79, v2
	v_mov_b32_e32 v80, v2
	v_mov_b32_e32 v81, v2
	v_mov_b32_e32 v82, v2
	v_mov_b32_e32 v83, v2
	v_mov_b32_e32 v84, v2
	v_mov_b32_e32 v85, v2
	v_mov_b32_e32 v86, v2
	v_mov_b32_e32 v87, v2
	v_mov_b32_e32 v88, v2
	v_mov_b32_e32 v89, v2
	v_mov_b32_e32 v90, v2
	v_mov_b32_e32 v91, v2
	v_mov_b32_e32 v92, v2
	v_mov_b32_e32 v93, v2
	v_mov_b32_e32 v94, v2
	v_mov_b32_e32 v95, v2
	v_mov_b32_e32 v96, v2
	v_mov_b32_e32 v97, v2
	v_mov_b32_e32 v34, v2
	v_mov_b32_e32 v35, v2
	v_mov_b32_e32 v36, v2
	v_mov_b32_e32 v37, v2
	v_mov_b32_e32 v38, v2
	v_mov_b32_e32 v39, v2
	v_mov_b32_e32 v40, v2
	v_mov_b32_e32 v41, v2
	v_mov_b32_e32 v42, v2
	v_mov_b32_e32 v43, v2
	v_mov_b32_e32 v44, v2
	v_mov_b32_e32 v45, v2
	v_mov_b32_e32 v46, v2
	v_mov_b32_e32 v47, v2
	v_mov_b32_e32 v48, v2
	v_mov_b32_e32 v49, v2
	v_mov_b32_e32 v50, v2
	v_mov_b32_e32 v51, v2
	v_mov_b32_e32 v52, v2
	v_mov_b32_e32 v53, v2
	v_mov_b32_e32 v54, v2
	v_mov_b32_e32 v55, v2
	v_mov_b32_e32 v56, v2
	v_mov_b32_e32 v57, v2
	v_mov_b32_e32 v58, v2
	v_mov_b32_e32 v59, v2
	v_mov_b32_e32 v60, v2
	v_mov_b32_e32 v61, v2
	v_mov_b32_e32 v62, v2
	v_mov_b32_e32 v63, v2
	v_mov_b32_e32 v64, v2
	v_mov_b32_e32 v65, v2
	v_mov_b32_e32 v98, v2
	v_mov_b32_e32 v99, v2
	v_mov_b32_e32 v100, v2
	v_mov_b32_e32 v101, v2
	v_mov_b32_e32 v102, v2
	v_mov_b32_e32 v103, v2
	v_mov_b32_e32 v104, v2
	v_mov_b32_e32 v105, v2
	v_mov_b32_e32 v106, v2
	v_mov_b32_e32 v107, v2
	v_mov_b32_e32 v108, v2
	v_mov_b32_e32 v109, v2
	v_mov_b32_e32 v110, v2
	v_mov_b32_e32 v111, v2
	v_mov_b32_e32 v112, v2
	v_mov_b32_e32 v113, v2
	v_mov_b32_e32 v114, v2
	v_mov_b32_e32 v115, v2
	v_mov_b32_e32 v116, v2
	v_mov_b32_e32 v117, v2
	v_mov_b32_e32 v118, v2
	v_mov_b32_e32 v119, v2
	v_mov_b32_e32 v120, v2
	v_mov_b32_e32 v121, v2
	v_mov_b32_e32 v122, v2
	v_mov_b32_e32 v123, v2
	v_mov_b32_e32 v124, v2
	v_mov_b32_e32 v125, v2
	v_mov_b32_e32 v126, v2
	v_mov_b32_e32 v127, v2
	v_mov_b32_e32 v128, v2
	v_mov_b32_e32 v129, v2
	.p2alignl 6, 3212836864

; template <bool MLA>
; __device__ __forceinline__ void attn_unit(const P& p, LAS unsigned char* lds, const int b, const int h, const int qb) {
;     ...
;     const int tid = threadIdx.x, wid = __builtin_amdgcn_readfirstlane(tid >> 6), lane = tid & 63, r32 = lane & 31, hi = lane >> 5;
;     const int q0 = qb * 256, qw = q0 + 32 * wid, qi = qw + r32, nt = (q0 + 256) / 64;
;     const bf16_t* Kn = MLA ? WSP(bf16_t, WS_KNOPE) : WSP(bf16_t, WS_SBK);
;     const bf16_t* Kr = WSP(bf16_t, WS_KROPE);
;     const bf16_t* Vt = WSP(bf16_t, MLA ? WS_VMT : WS_SBVT) + (size_t)(b * 8 + h) * 128 * SEQ;
;     LAS float* al = (LAS float*)(lds + LDS_AL) + wid * 32;
;     LAS int* flag = (LAS int*)(lds + LDS_FLAG);
;     bf16x8 qf[NQF];
;     { const char* qb_ = MLA ? (const char*)WSP(bf16_t, WS_QMLA) + ((size_t)(b * SEQ + qw) * 1536 + h * 192) * 2 : (const char*)WSP(bf16_t, WS_SBQ) + ((size_t)(b * SEQ + qw) * 1024 + h * 128) * 2;
;       const unsigned qo = (unsigned)((r32 * (MLA ? 1536 : 1024) + 8 * hi) * 2);
; #pragma unroll
;       for (int s = 0; s < NQF; ++s) qf[s] = *(const bf16x8*)(qb_ + qo + 32 * s); }
;     bf16x8 tri0, tri1, ones;
; #pragma unroll
;     for (int j = 0; j < 8; ++j) { const int k0_ = 8 * (j >> 2) + 4 * hi + (j & 3); tri0[j] = (k0_ > r32) ? (short)0x3F80 : (short)0; tri1[j] = (16 + k0_ > r32) ? (short)0x3F80 : (short)0; ones[j] = (short)0x3F80; }
;     u32x4 kreg[NKR], vreg[2];
;     const unsigned kofs0 = (unsigned)(((tid >> 4) * 1024 + (tid & 15) * 8) * 2), kofs1 = kofs0 + 32u * 1024u * 2u;
;     const unsigned rofs = (unsigned)(((tid >> 3) * 64 + (tid & 7) * 8) * 2);
;     const unsigned vofs0 = (unsigned)(((tid >> 3) * SEQ + (tid & 7) * 8) * 2), vofs1 = vofs0 + 64u * SEQ * 2u;
;     const unsigned kw0 = (unsigned)((tid >> 4) * KSTR + (tid & 15) * 16), kw1 = kw0 + 32u * KSTR, rw = (unsigned)((tid >> 3) * KSTR + 256 + (tid & 7) * 16);
;     const unsigned vw0 = (unsigned)(KT + (tid >> 3) * VSTR + (16 * ((tid & 7) >> 1) + 4 * (tid & 1)) * 2), vw1 = vw0 + 64u * VSTR;
;     const char* Knb = (const char*)Kn + ((size_t)b * SEQ * 1024 + h * 128) * 2; const char* Krb = (const char*)Kr + (size_t)b * SEQ * 64 * 2; const char* Vtb = (const char*)Vt;
;     ...
;     f32x16 o[4];
; #pragma unroll
;     for (int d0 = 0; d0 < 4; ++d0)
; #pragma unroll
;         for (int r = 0; r < 16; ++r) o[d0][r] = 0.f;
;     float m_run = -1e30f, l_run = 0.f, R2 = 0.f;
.LBB0_705:
	v_readlane_b32 s8, v242, 40
	s_bfe_u32 s1, s2, 0x40001
	s_lshr_b32 s2, s2, 5
	v_readlane_b32 s9, v242, 41
	s_and_b64 s[8:9], s[8:9], exec
	s_cselect_b32 s1, s1, s2
	v_readfirstlane_b32 s2, v0
	s_lshl_b32 s13, s1, 8
	s_lshr_b32 s1, s2, 1
	s_and_b32 s14, s1, 0x7fffffe0
	s_sub_i32 s93, s14, s13
	s_ashr_i32 s1, s0, 31
	s_ashr_i32 s8, s0, 3
	s_and_b32 s12, s0, 7
	s_add_i32 s2, s93, 0xf00
	s_sub_i32 s9, 0x1000, s13
	s_lshl_b64 s[0:1], s[0:1], 20
	s_add_u32 s0, s88, s0
	s_addc_u32 s1, s89, s1
	s_lshl_b32 s10, s8, 12
	s_add_i32 s82, s2, s10
	s_mul_i32 s10, s82, 0x600
	s_mul_i32 s15, s12, 0xc0
	s_mul_hi_i32 s11, s82, 0x600
	s_or_b32 s10, s10, s15
	s_lshr_b32 s92, s9, 6
	s_ashr_i32 s9, s8, 31
	s_ashr_i32 s83, s82, 31
	v_lshl_add_u64 v[4:5], s[10:11], 1, v[188:189]
	s_lshl_b32 s90, s12, 7
	s_lshl_b64 s[10:11], s[8:9], 23
	s_add_u32 s10, s76, s10
	s_addc_u32 s11, s77, s11
	s_lshl_b32 s15, s14, 2
	s_add_i32 s91, s15, 0
	s_lshl_b64 s[8:9], s[8:9], 19
	s_add_i32 s91, s91, 0x16000
	s_lshl_b32 s12, s12, 8
	s_add_u32 s10, s10, s12
	s_addc_u32 s11, s11, 0
	global_load_dwordx4 v[114:117], v[4:5], off offset:32
	global_load_dwordx4 v[118:121], v[4:5], off offset:64
	global_load_dwordx4 v[122:125], v[4:5], off offset:96
	global_load_dwordx4 v[126:129], v[4:5], off offset:128
	v_lshl_add_u64 v[192:193], s[10:11], 0, v[182:183]
	s_mov_b32 s10, 0x10000
	v_add_co_u32_e32 v6, vcc, s10, v192
	v_lshl_add_u64 v[194:195], v[190:191], 0, s[8:9]
	s_nop 0
	v_addc_co_u32_e32 v7, vcc, 0, v193, vcc
	global_load_dwordx4 v[130:133], v[4:5], off offset:352
	global_load_dwordx4 v[142:145], v[6:7], off
	global_load_dwordx4 v[138:141], v[192:193], off
	global_load_dwordx4 v[170:173], v[194:195], off
	v_lshl_add_u64 v[196:197], s[0:1], 0, v[184:185]
	global_load_dwordx4 v[134:137], v[4:5], off
	global_load_dwordx4 v[174:177], v[196:197], off
	s_mov_b32 s0, 0x80000
	v_add_co_u32_e32 v6, vcc, s0, v196
	s_waitcnt vmcnt(10)
	v_mov_b32_e32 v16, v2
	v_addc_co_u32_e32 v7, vcc, 0, v197, vcc
	global_load_dwordx4 v[178:181], v[6:7], off
	global_load_dwordx4 v[146:149], v[4:5], off offset:160
	global_load_dwordx4 v[150:153], v[4:5], off offset:192
	global_load_dwordx4 v[154:157], v[4:5], off offset:224
	global_load_dwordx4 v[158:161], v[4:5], off offset:256
	global_load_dwordx4 v[162:165], v[4:5], off offset:288
	global_load_dwordx4 v[166:169], v[4:5], off offset:320
	v_mov_b32_e32 v17, v2
	v_add_u32_e32 v50, s14, v205
	v_mov_b32_e32 v3, v2
	v_mov_b32_e32 v4, v2
	v_mov_b32_e32 v5, v2
	v_mov_b32_e32 v6, v2
	v_mov_b32_e32 v7, v2
	v_mov_b32_e32 v8, v2
	v_mov_b32_e32 v9, v2
	v_mov_b32_e32 v10, v2
	v_mov_b32_e32 v11, v2
	v_mov_b32_e32 v12, v2
	v_mov_b32_e32 v13, v2
	v_mov_b32_e32 v14, v2
	v_mov_b32_e32 v15, v2
	v_mov_b64_e32 v[32:33], v[16:17]
	v_mov_b64_e32 v[48:49], v[16:17]
	v_subrev_u32_e32 v213, s13, v50
	v_mov_b64_e32 v[64:65], v[16:17]
	v_mov_b64_e32 v[80:81], v[16:17]
	s_mov_b32 s0, 0
	v_mov_b32_e32 v215, 0
	v_mov_b32_e32 v216, 0xf149f2ca
	s_mov_b32 s84, 64
	v_mov_b64_e32 v[30:31], v[14:15]
	v_mov_b64_e32 v[28:29], v[12:13]
	v_mov_b64_e32 v[26:27], v[10:11]
	v_mov_b64_e32 v[24:25], v[8:9]
	v_mov_b64_e32 v[22:23], v[6:7]
	v_mov_b64_e32 v[20:21], v[4:5]
	v_mov_b64_e32 v[18:19], v[2:3]
	v_mov_b64_e32 v[46:47], v[14:15]
	v_mov_b64_e32 v[44:45], v[12:13]
	v_mov_b64_e32 v[42:43], v[10:11]
	v_mov_b64_e32 v[40:41], v[8:9]
	v_mov_b64_e32 v[38:39], v[6:7]
	v_mov_b64_e32 v[36:37], v[4:5]
	v_mov_b64_e32 v[34:35], v[2:3]
	v_lshl_add_u32 v212, v1, 2, s91
	v_lshl_add_u32 v214, v203, 2, s91
	s_addk_i32 s93, 0xf1f
	v_mov_b64_e32 v[62:63], v[14:15]
	v_mov_b64_e32 v[60:61], v[12:13]
	v_mov_b64_e32 v[58:59], v[10:11]
	v_mov_b64_e32 v[56:57], v[8:9]
	v_mov_b64_e32 v[54:55], v[6:7]
	v_mov_b64_e32 v[52:53], v[4:5]
	v_mov_b64_e32 v[50:51], v[2:3]
	v_mov_b64_e32 v[78:79], v[14:15]
	v_mov_b64_e32 v[76:77], v[12:13]
	v_mov_b64_e32 v[74:75], v[10:11]
	v_mov_b64_e32 v[72:73], v[8:9]
	v_mov_b64_e32 v[70:71], v[6:7]
	v_mov_b64_e32 v[68:69], v[4:5]
	v_mov_b64_e32 v[66:67], v[2:3]
	s_waitcnt vmcnt(10)
	ds_write_b128 v206, v[138:141]
	ds_write_b128 v206, v[142:145] offset:12800
	s_waitcnt vmcnt(9)
	ds_write_b128 v207, v[170:173] offset:256
	s_waitcnt vmcnt(7)
	ds_write2_b64 v208, v[174:175], v[176:177] offset0:128 offset1:130
	s_waitcnt vmcnt(0)
	ds_write2_b64 v209, v[178:179], v[180:181] offset1:2
	s_waitcnt lgkmcnt(0)
	s_barrier
	.p2alignl 6, 3212836864

; template <bool MLA>
; __device__ __forceinline__ void attn_unit(const P& p, LAS unsigned char* lds, const int b, const int h, const int qb) {
;     ...
;     for (int it = 0; it < nt; ++it) {
;         const int tile = MLA ? it : nt - 1 - it, cb = it & 1, k0 = tile * 64;
;         const bool more = it + 1 < nt;
;         if (more) AT_LOAD(MLA ? tile + 1 : tile - 1);
;         const bool active = MLA ? (k0 <= qw + 31) : (k0 < qw + 31 && !__all(R2 < -160.f));
;         if (active) {
;     ...
;         if (!MLA) { int all = 1;
; #pragma unroll
;             for (int w8 = 0; w8 < 8; ++w8) all &= flag[w8];
;             if (all) break; }
;     }
.LBB0_741:
	s_cbranch_execz .LBB0_754
	s_branch .LBB0_729
	.p2alignl 6, 3212836864

;     __device__ bool next(int i, Unit& u) const { const int L = i * G + c; if (L >= 256) return false; u.pm = L >> 2; u.pn = L & 3; u.pb = 16; u.e = 0; u.ko = (L & 3) * 1024; u.ui = i; return true; }
;     __device__ bool next(int i, Unit& u) const {
;         const long L = (long)i * G + c; if (L >= nwg) return false;
;         int wgid = (int)L; { const int q = nwg / NXCD, r = nwg % NXCD, xcd = wgid % NXCD, off = wgid / NXCD; wgid = (xcd < r ? xcd * (q + 1) : r * (q + 1) + (xcd - r) * q) + off; }
;         const int nig = WGM * nN, gid = wgid / nig, fm = gid * WGM, gsz = (nM - fm) < WGM ? (nM - fm) : WGM;
;         u.pm = fm + ((wgid % nig) % gsz); u.pn = (wgid % nig) / gsz; u.pb = u.pn >= skip_from ? u.pn + skip_by : u.pn; u.e = 0; u.ko = 0; u.ui = i; return true;
;     ...
;     for (;;) {
;         const bool has_next = S.next(ui + 1, nxt);
;         const char* nB = has_next ? (const char*)Bt + (size_t)nxt.pb * tstep + nxt.ko : (chain ? cBn : cB);
;         int t0 = 0;
;         if (Epi::NST > 0 && ui > 0) { PG_KPAIR(0, 8 + Epi::NST); t0 = 2; }
;         for (int t = t0; t < nt; t += 2) PG_KPAIR(t, 8);
;         E(acc, cur, wr, wc, fr, fq);
;         if (!has_next) break;
; #pragma unroll
;         for (int a = 0; a < 2; ++a)
; #pragma unroll
;             for (int b = 0; b < 2; ++b)
; #pragma unroll
;                 for (int m = 0; m < 4; ++m)
; #pragma unroll
;                     for (int n = 0; n < 2; ++n) acc[a][b][m][n] = (f32x4){0.f, 0.f, 0.f, 0.f};
;         cur = nxt; cB = nB; ++ui;
.LBB0_994:
	s_ashr_i32 s13, s12, 31
	s_lshl_b64 s[14:15], s[12:13], 20
	s_add_u32 s14, s25, s14
	v_lshl_or_b32 v2, s47, 8, v198
	s_addc_u32 s15, s26, s15
	v_or_b32_e32 v3, v2, v199
	v_or_b32_e32 v2, v2, v200
	s_and_b64 s[18:19], exec, s[4:5]
	v_lshlrev_b32_e32 v2, 12, v2
	s_cselect_b32 s13, s17, s15
	s_cselect_b32 s49, s16, s14
	v_lshl_or_b32 v212, v3, 12, v1
	v_or_b32_e32 v214, v2, v1
	v_add_u32_e32 v215, v2, v206
	s_add_u32 s50, s16, 0x100
	v_mov_b32_e32 v2, 0
	v_or_b32_e32 v213, 0x80000, v212
	s_addc_u32 s51, s17, 0
	s_mov_b32 s52, -2
	s_mov_b64 s[16:17], 0
	v_mov_b32_e32 v3, v2
	v_mov_b32_e32 v4, v2
	v_mov_b32_e32 v5, v2
	v_mov_b32_e32 v6, v2
	v_mov_b32_e32 v7, v2
	v_mov_b32_e32 v8, v2
	v_mov_b32_e32 v9, v2
	s_waitcnt vmcnt(1)
	v_mov_b32_e32 v10, v2
	v_mov_b32_e32 v11, v2
	v_mov_b32_e32 v12, v2
	v_mov_b32_e32 v13, v2
	v_mov_b32_e32 v18, v2
	v_mov_b32_e32 v19, v2
	v_mov_b32_e32 v20, v2
	v_mov_b32_e32 v21, v2
	v_mov_b32_e32 v26, v2
	v_mov_b32_e32 v27, v2
	v_mov_b32_e32 v28, v2
	v_mov_b32_e32 v29, v2
	v_mov_b32_e32 v34, v2
	v_mov_b32_e32 v35, v2
	v_mov_b32_e32 v36, v2
	v_mov_b32_e32 v37, v2
	v_mov_b32_e32 v42, v2
	v_mov_b32_e32 v43, v2
	v_mov_b32_e32 v44, v2
	v_mov_b32_e32 v45, v2
	s_waitcnt vmcnt(0)
	v_mov_b32_e32 v50, v2
	v_mov_b32_e32 v51, v2
	v_mov_b32_e32 v52, v2
	v_mov_b32_e32 v53, v2
	v_mov_b32_e32 v14, v2
	v_mov_b32_e32 v15, v2
	v_mov_b32_e32 v16, v2
	v_mov_b32_e32 v17, v2
	v_mov_b32_e32 v22, v2
	v_mov_b32_e32 v23, v2
	v_mov_b32_e32 v24, v2
	v_mov_b32_e32 v25, v2
	v_mov_b32_e32 v30, v2
	v_mov_b32_e32 v31, v2
	v_mov_b32_e32 v32, v2
	v_mov_b32_e32 v33, v2
	v_mov_b32_e32 v38, v2
	v_mov_b32_e32 v39, v2
	v_mov_b32_e32 v40, v2
	v_mov_b32_e32 v41, v2
	v_mov_b32_e32 v46, v2
	v_mov_b32_e32 v47, v2
	v_mov_b32_e32 v48, v2
	v_mov_b32_e32 v49, v2
	v_mov_b32_e32 v54, v2
	v_mov_b32_e32 v55, v2
	v_mov_b32_e32 v56, v2
	v_mov_b32_e32 v57, v2
	v_mov_b32_e32 v58, v2
	v_mov_b32_e32 v59, v2
	v_mov_b32_e32 v60, v2
	v_mov_b32_e32 v61, v2
	v_mov_b32_e32 v62, v2
	v_mov_b32_e32 v63, v2
	v_mov_b32_e32 v64, v2
	v_mov_b32_e32 v65, v2
	v_mov_b32_e32 v66, v2
	v_mov_b32_e32 v67, v2
	v_mov_b32_e32 v68, v2
	v_mov_b32_e32 v69, v2
	v_mov_b32_e32 v70, v2
	v_mov_b32_e32 v71, v2
	v_mov_b32_e32 v72, v2
	v_mov_b32_e32 v73, v2
	v_mov_b32_e32 v74, v2
	v_mov_b32_e32 v75, v2
	v_mov_b32_e32 v76, v2
	v_mov_b32_e32 v77, v2
	v_mov_b32_e32 v82, v2
	v_mov_b32_e32 v83, v2
	v_mov_b32_e32 v84, v2
	v_mov_b32_e32 v85, v2
	v_mov_b32_e32 v98, v2
	v_mov_b32_e32 v99, v2
	v_mov_b32_e32 v100, v2
	v_mov_b32_e32 v101, v2
	v_mov_b32_e32 v102, v2
	v_mov_b32_e32 v103, v2
	v_mov_b32_e32 v104, v2
	v_mov_b32_e32 v105, v2
	v_mov_b32_e32 v106, v2
	v_mov_b32_e32 v107, v2
	v_mov_b32_e32 v108, v2
	v_mov_b32_e32 v109, v2
	v_mov_b32_e32 v110, v2
	v_mov_b32_e32 v111, v2
	v_mov_b32_e32 v112, v2
	v_mov_b32_e32 v113, v2
	v_mov_b32_e32 v78, v2
	v_mov_b32_e32 v79, v2
	v_mov_b32_e32 v80, v2
	v_mov_b32_e32 v81, v2
	v_mov_b32_e32 v86, v2
	v_mov_b32_e32 v87, v2
	v_mov_b32_e32 v88, v2
	v_mov_b32_e32 v89, v2
	v_mov_b32_e32 v90, v2
	v_mov_b32_e32 v91, v2
	v_mov_b32_e32 v92, v2
	v_mov_b32_e32 v93, v2
	v_mov_b32_e32 v94, v2
	v_mov_b32_e32 v95, v2
	v_mov_b32_e32 v96, v2
	v_mov_b32_e32 v97, v2
	v_mov_b32_e32 v114, v2
	v_mov_b32_e32 v115, v2
	v_mov_b32_e32 v116, v2
	v_mov_b32_e32 v117, v2
	v_mov_b32_e32 v118, v2
	v_mov_b32_e32 v119, v2
	v_mov_b32_e32 v120, v2
	v_mov_b32_e32 v121, v2
	v_mov_b32_e32 v122, v2
	v_mov_b32_e32 v123, v2
	v_mov_b32_e32 v124, v2
	v_mov_b32_e32 v125, v2
	v_mov_b32_e32 v126, v2
	v_mov_b32_e32 v127, v2
	v_mov_b32_e32 v128, v2
	v_mov_b32_e32 v129, v2
	.p2alignl 6, 3212836864

;     __device__ bool next(int i, Unit& u) const { const int L = i * G + c; if (L >= 256) return false; u.pm = L >> 2; u.pn = L & 3; u.pb = 16; u.e = 0; u.ko = (L & 3) * 1024; u.ui = i; return true; }
;     ...
;     for (;;) {
;         const bool has_next = S.next(ui + 1, nxt);
;         const char* nB = has_next ? (const char*)Bt + (size_t)nxt.pb * tstep + nxt.ko : (chain ? cBn : cB);
;         int t0 = 0;
;         if (Epi::NST > 0 && ui > 0) { PG_KPAIR(0, 8 + Epi::NST); t0 = 2; }
;         for (int t = t0; t < nt; t += 2) PG_KPAIR(t, 8);
;         E(acc, cur, wr, wc, fr, fq);
;         if (!has_next) break;
; #pragma unroll
;         for (int a = 0; a < 2; ++a)
; #pragma unroll
;             for (int b = 0; b < 2; ++b)
; #pragma unroll
;                 for (int m = 0; m < 4; ++m)
; #pragma unroll
;                     for (int n = 0; n < 2; ++n) acc[a][b][m][n] = (f32x4){0.f, 0.f, 0.f, 0.f};
;         cur = nxt; cB = nB; ++ui;
.LBB0_1998:
	s_ashr_i32 s23, s22, 31
	s_lshl_b64 s[26:27], s[22:23], 19
	s_add_u32 s26, s45, s26
	s_addc_u32 s27, s46, s27
	s_and_b64 s[30:31], exec, s[18:19]
	s_cselect_b32 s2, s7, s27
	s_cselect_b32 s23, s6, s26
	s_add_i32 s33, s28, -2
	s_lshl_b32 s40, s28, 7
	v_lshl_add_u32 v2, s89, 9, v216
	s_add_u32 s41, s6, 0x100
	v_lshl_add_u32 v230, v217, 1, v2
	v_lshl_add_u32 v231, v218, 1, v2
	s_addc_u32 s76, s7, 0
	s_mov_b64 s[28:29], 0x1f740000
	s_mov_b64 s[30:31], s[4:5]
	s_branch .LBB0_2000
	.p2alignl 6, 3212836864

;     __device__ bool next(int i, Unit& u) const { const int L = i * G + c; if (L >= 256) return false; u.pm = L >> 2; u.pn = L & 3; u.pb = 16; u.e = 0; u.ko = (L & 3) * 1024; u.ui = i; return true; }
;     ...
;     for (;;) {
;         const bool has_next = S.next(ui + 1, nxt);
;         const char* nB = has_next ? (const char*)Bt + (size_t)nxt.pb * tstep + nxt.ko : (chain ? cBn : cB);
;         int t0 = 0;
;         if (Epi::NST > 0 && ui > 0) { PG_KPAIR(0, 8 + Epi::NST); t0 = 2; }
;         for (int t = t0; t < nt; t += 2) PG_KPAIR(t, 8);
;         E(acc, cur, wr, wc, fr, fq);
;         if (!has_next) break;
; #pragma unroll
;         for (int a = 0; a < 2; ++a)
; #pragma unroll
;             for (int b = 0; b < 2; ++b)
; #pragma unroll
;                 for (int m = 0; m < 4; ++m)
; #pragma unroll
;                     for (int n = 0; n < 2; ++n) acc[a][b][m][n] = (f32x4){0.f, 0.f, 0.f, 0.f};
;         cur = nxt; cB = nB; ++ui;
;     __device__ bool next(int i, Unit& u) const {
;     ...
;         u.pm = g; u.pn = ct; u.pb = e * NCT + ct; u.e = e; u.ko = 0; u.ui = i; return true;
;     }
.LBB0_2902:
	s_ashr_i32 s29, s28, 31
	s_lshl_b64 s[30:31], s[28:29], 19
	s_add_u32 s30, s47, s30
	s_addc_u32 s31, s48, s31
	s_and_b64 s[36:37], exec, s[24:25]
	v_lshl_or_b32 v2, s23, 8, v200
	s_cselect_b32 s2, s9, s31
	s_cselect_b32 s29, s8, s30
	v_or_b32_e32 v3, v2, v201
	v_or_b32_e32 v2, v2, v203
	s_add_i32 s33, s34, -2
	s_lshl_b32 s40, s34, 7
	v_lshl_or_b32 v216, v3, 11, v1
	v_lshlrev_b32_e32 v2, 11, v2
	s_add_u32 s41, s8, 0x100
	v_or_b32_e32 v217, 0x40000, v216
	v_or_b32_e32 v218, v2, v1
	v_add_u32_e32 v219, v2, v209
	s_addc_u32 s76, s9, 0
	s_mov_b64 s[34:35], 0x23a00000
	s_mov_b64 s[36:37], s[6:7]
	s_branch .LBB0_2904
	.p2alignl 6, 3212836864
